# remaining flat_store_dwordx4 (bf16 GEMM epilogues, attention outputs) replaced by global_store_dwordx4, on top of the expert-GEMM epilogue change
# speedup vs baseline: 1.0139x; 1.0104x over previous
.LBB0_146:
	v_add_u32_e32 v139, s16, v135
	v_mad_u64_u32 v[142:143], s[20:21], v139, s26, 0
	v_cvt_pk_bf16_f32 v114, v114, v115
	v_cvt_pk_bf16_f32 v115, v116, v117
	v_cvt_pk_bf16_f32 v116, v106, v107
	v_add_u32_e32 v106, 16, v139
	v_ashrrev_i32_e32 v145, 31, v139
	v_mov_b32_e32 v144, v143
	v_cvt_pk_bf16_f32 v117, v108, v109
	v_ashrrev_i32_e32 v109, 31, v106
	v_mad_u64_u32 v[106:107], s[20:21], v106, s26, 0
	v_cvt_pk_bf16_f32 v98, v98, v99
	v_cvt_pk_bf16_f32 v99, v100, v101
	v_cvt_pk_bf16_f32 v100, v90, v91
	v_add_u32_e32 v90, 32, v139
	v_add_u32_e32 v140, s46, v137
	v_mad_u64_u32 v[144:145], s[20:21], v145, s26, v[144:145]
	v_mov_b32_e32 v108, v107
	v_cvt_pk_bf16_f32 v101, v92, v93
	v_ashrrev_i32_e32 v93, 31, v90
	v_mad_u64_u32 v[90:91], s[20:21], v90, s26, 0
	v_cvt_pk_bf16_f32 v82, v82, v83
	v_cvt_pk_bf16_f32 v83, v84, v85
	v_cvt_pk_bf16_f32 v84, v74, v75
	v_add_u32_e32 v74, 48, v139
	v_cvt_pk_bf16_f32 v70, v70, v71
	v_cvt_pk_bf16_f32 v71, v72, v73
	v_cvt_pk_bf16_f32 v72, v66, v67
	v_add_u32_e32 v66, 0x80, v139
	v_ashrrev_i32_e32 v141, 31, v140
	v_mov_b32_e32 v143, v144
	v_mad_u64_u32 v[108:109], s[20:21], v109, s26, v[108:109]
	v_mov_b32_e32 v92, v91
	v_cvt_pk_bf16_f32 v85, v76, v77
	v_ashrrev_i32_e32 v77, 31, v74
	v_mad_u64_u32 v[74:75], s[20:21], v74, s26, 0
	v_cvt_pk_bf16_f32 v73, v68, v69
	v_ashrrev_i32_e32 v69, 31, v66
	v_mad_u64_u32 v[66:67], s[20:21], v66, s26, 0
	v_cvt_pk_bf16_f32 v50, v50, v51
	v_cvt_pk_bf16_f32 v51, v52, v53
	v_cvt_pk_bf16_f32 v52, v42, v43
	v_add_u32_e32 v42, 0x90, v139
	v_lshl_add_u64 v[142:143], v[142:143], 1, s[8:9]
	v_lshlrev_b64 v[140:141], 1, v[140:141]
	v_mov_b32_e32 v107, v108
	v_mad_u64_u32 v[92:93], s[20:21], v93, s26, v[92:93]
	v_mov_b32_e32 v76, v75
	v_mov_b32_e32 v68, v67
	v_cvt_pk_bf16_f32 v53, v44, v45
	v_ashrrev_i32_e32 v45, 31, v42
	v_mad_u64_u32 v[42:43], s[20:21], v42, s26, 0
	v_cvt_pk_bf16_f32 v34, v34, v35
	v_cvt_pk_bf16_f32 v35, v36, v37
	v_cvt_pk_bf16_f32 v36, v26, v27
	v_add_u32_e32 v26, 0xa0, v139
	v_lshl_add_u64 v[142:143], v[142:143], 0, v[140:141]
	v_lshl_add_u64 v[106:107], v[106:107], 1, s[8:9]
	v_mov_b32_e32 v91, v92
	v_mad_u64_u32 v[76:77], s[20:21], v77, s26, v[76:77]
	v_mad_u64_u32 v[68:69], s[20:21], v69, s26, v[68:69]
	v_mov_b32_e32 v44, v43
	v_cvt_pk_bf16_f32 v37, v28, v29
	v_ashrrev_i32_e32 v29, 31, v26
	v_mad_u64_u32 v[26:27], s[20:21], v26, s26, 0
	v_cvt_pk_bf16_f32 v18, v18, v19
	v_cvt_pk_bf16_f32 v19, v20, v21
	v_cvt_pk_bf16_f32 v20, v10, v11
	v_add_u32_e32 v10, 0xb0, v139
	v_cvt_pk_bf16_f32 v126, v126, v127
	v_cvt_pk_bf16_f32 v127, v128, v129
	v_cvt_pk_bf16_f32 v128, v122, v123
	v_cvt_pk_bf16_f32 v129, v124, v125
	global_store_dwordx4 v[142:143], v[114:117], off offset:256
	v_lshl_add_u64 v[90:91], v[90:91], 1, s[8:9]
	v_mov_b32_e32 v75, v76
	v_lshl_add_u64 v[114:115], v[106:107], 0, v[140:141]
	v_mov_b32_e32 v67, v68
	v_mad_u64_u32 v[44:45], s[20:21], v45, s26, v[44:45]
	v_mov_b32_e32 v28, v27
	v_cvt_pk_bf16_f32 v21, v12, v13
	v_ashrrev_i32_e32 v13, 31, v10
	v_mad_u64_u32 v[10:11], s[20:21], v10, s26, 0
	global_store_dwordx4 v[142:143], v[126:129], off
	v_cvt_pk_bf16_f32 v106, v118, v119
	v_cvt_pk_bf16_f32 v107, v120, v121
	v_cvt_pk_bf16_f32 v108, v110, v111
	v_cvt_pk_bf16_f32 v109, v112, v113
	global_store_dwordx4 v[114:115], v[98:101], off offset:256
	v_lshl_add_u64 v[74:75], v[74:75], 1, s[8:9]
	v_lshl_add_u64 v[66:67], v[66:67], 1, s[8:9]
	v_lshl_add_u64 v[98:99], v[90:91], 0, v[140:141]
	v_mov_b32_e32 v43, v44
	v_mad_u64_u32 v[28:29], s[20:21], v29, s26, v[28:29]
	v_mov_b32_e32 v12, v11
	global_store_dwordx4 v[114:115], v[106:109], off
	v_cvt_pk_bf16_f32 v90, v102, v103
	v_cvt_pk_bf16_f32 v91, v104, v105
	v_cvt_pk_bf16_f32 v92, v94, v95
	v_cvt_pk_bf16_f32 v93, v96, v97
	global_store_dwordx4 v[98:99], v[82:85], off offset:256
	v_cvt_pk_bf16_f32 v76, v78, v79
	v_cvt_pk_bf16_f32 v77, v80, v81
	v_lshl_add_u64 v[82:83], v[74:75], 0, v[140:141]
	v_cvt_pk_bf16_f32 v74, v86, v87
	v_cvt_pk_bf16_f32 v75, v88, v89
	v_lshl_add_u64 v[66:67], v[66:67], 0, v[140:141]
	v_lshl_add_u64 v[42:43], v[42:43], 1, s[8:9]
	v_mov_b32_e32 v27, v28
	v_mad_u64_u32 v[12:13], s[20:21], v13, s26, v[12:13]
	global_store_dwordx4 v[98:99], v[90:93], off
	global_store_dwordx4 v[82:83], v[74:77], off
	global_store_dwordx4 v[82:83], v[70:73], off offset:256
	v_cvt_pk_bf16_f32 v62, v62, v63
	v_cvt_pk_bf16_f32 v63, v64, v65
	v_cvt_pk_bf16_f32 v64, v58, v59
	v_cvt_pk_bf16_f32 v65, v60, v61
	global_store_dwordx4 v[66:67], v[50:53], off offset:256
	v_lshl_add_u64 v[26:27], v[26:27], 1, s[8:9]
	v_mov_b32_e32 v11, v12
	v_lshl_add_u64 v[50:51], v[42:43], 0, v[140:141]
	global_store_dwordx4 v[66:67], v[62:65], off
	v_cvt_pk_bf16_f32 v42, v54, v55
	v_cvt_pk_bf16_f32 v43, v56, v57
	v_cvt_pk_bf16_f32 v44, v46, v47
	v_cvt_pk_bf16_f32 v45, v48, v49
	global_store_dwordx4 v[50:51], v[34:37], off offset:256
	v_lshl_add_u64 v[10:11], v[10:11], 1, s[8:9]
	global_store_dwordx4 v[50:51], v[42:45], off
	v_lshl_add_u64 v[34:35], v[26:27], 0, v[140:141]
	v_cvt_pk_bf16_f32 v26, v38, v39
	v_cvt_pk_bf16_f32 v27, v40, v41
	v_cvt_pk_bf16_f32 v28, v30, v31
	v_cvt_pk_bf16_f32 v29, v32, v33
	global_store_dwordx4 v[34:35], v[18:21], off offset:256
	v_cvt_pk_bf16_f32 v12, v14, v15
	v_cvt_pk_bf16_f32 v13, v16, v17
	v_lshl_add_u64 v[18:19], v[10:11], 0, v[140:141]
	v_cvt_pk_bf16_f32 v10, v22, v23
	v_cvt_pk_bf16_f32 v11, v24, v25
	v_cvt_pk_bf16_f32 v6, v6, v7
	v_cvt_pk_bf16_f32 v7, v8, v9
	v_cvt_pk_bf16_f32 v8, v2, v3
	v_cvt_pk_bf16_f32 v9, v4, v5
	s_andn2_b64 vcc, exec, s[2:3]
	s_mov_b64 s[2:3], -1
	global_store_dwordx4 v[34:35], v[26:29], off
	global_store_dwordx4 v[18:19], v[10:13], off
	global_store_dwordx4 v[18:19], v[6:9], off offset:256
	s_cbranch_vccnz .LBB0_139
	s_andn2_b64 vcc, exec, s[6:7]
	s_cbranch_vccnz .LBB0_138
	s_barrier
	s_branch .LBB0_138

.LBB0_171:
	v_add_u32_e32 v138, s6, v133
	v_ashrrev_i32_e32 v139, 31, v138
	v_add_u32_e32 v140, s37, v135
	v_lshlrev_b64 v[138:139], 15, v[138:139]
	v_ashrrev_i32_e32 v141, 31, v140
	v_lshl_add_u64 v[138:139], s[4:5], 0, v[138:139]
	v_lshl_add_u64 v[138:139], v[140:141], 1, v[138:139]
	v_cvt_pk_bf16_f32 v110, v110, v111
	v_cvt_pk_bf16_f32 v111, v112, v113
	v_cvt_pk_bf16_f32 v112, v106, v107
	v_cvt_pk_bf16_f32 v113, v108, v109
	s_mov_b32 s6, 0x80000
	global_store_dwordx4 v[138:139], v[110:113], off offset:256
	s_mov_b64 s[16:17], 0x80000
	v_cvt_pk_bf16_f32 v94, v94, v95
	v_add_co_u32_e32 v112, vcc, s6, v138
	v_lshl_add_u64 v[110:111], v[138:139], 0, s[16:17]
	s_nop 0
	v_addc_co_u32_e32 v113, vcc, 0, v139, vcc
	v_cvt_pk_bf16_f32 v95, v96, v97
	v_cvt_pk_bf16_f32 v96, v90, v91
	v_cvt_pk_bf16_f32 v97, v92, v93
	s_mov_b32 s6, 0x100000
	global_store_dwordx4 v[110:111], v[94:97], off offset:256
	s_mov_b64 s[16:17], 0x100000
	v_cvt_pk_bf16_f32 v78, v78, v79
	v_add_co_u32_e32 v96, vcc, s6, v138
	v_lshl_add_u64 v[94:95], v[138:139], 0, s[16:17]
	s_nop 0
	v_addc_co_u32_e32 v97, vcc, 0, v139, vcc
	v_cvt_pk_bf16_f32 v79, v80, v81
	v_cvt_pk_bf16_f32 v80, v74, v75
	v_cvt_pk_bf16_f32 v81, v76, v77
	s_mov_b32 s6, 0x180000
	global_store_dwordx4 v[94:95], v[78:81], off offset:256
	s_mov_b64 s[16:17], 0x180000
	v_cvt_pk_bf16_f32 v70, v70, v71
	v_add_co_u32_e32 v80, vcc, s6, v138
	s_mov_b32 s6, 0x400000
	s_nop 0
	v_addc_co_u32_e32 v81, vcc, 0, v139, vcc
	v_lshl_add_u64 v[78:79], v[138:139], 0, s[16:17]
	v_cvt_pk_bf16_f32 v71, v72, v73
	v_cvt_pk_bf16_f32 v72, v62, v63
	v_cvt_pk_bf16_f32 v73, v64, v65
	s_mov_b64 s[16:17], 0x400000
	v_cvt_pk_bf16_f32 v64, v58, v59
	v_add_co_u32_e32 v58, vcc, s6, v138
	global_store_dwordx4 v[78:79], v[70:73], off offset:256
	s_nop 0
	v_addc_co_u32_e32 v59, vcc, 0, v139, vcc
	v_lshl_add_u64 v[70:71], v[138:139], 0, s[16:17]
	v_cvt_pk_bf16_f32 v46, v46, v47
	v_cvt_pk_bf16_f32 v47, v48, v49
	v_cvt_pk_bf16_f32 v48, v42, v43
	v_cvt_pk_bf16_f32 v49, v44, v45
	s_mov_b32 s6, 0x480000
	global_store_dwordx4 v[70:71], v[46:49], off offset:256
	s_mov_b64 s[16:17], 0x480000
	v_cvt_pk_bf16_f32 v30, v30, v31
	v_add_co_u32_e32 v48, vcc, s6, v138
	v_lshl_add_u64 v[46:47], v[138:139], 0, s[16:17]
	s_nop 0
	v_addc_co_u32_e32 v49, vcc, 0, v139, vcc
	v_cvt_pk_bf16_f32 v31, v32, v33
	v_cvt_pk_bf16_f32 v32, v26, v27
	v_cvt_pk_bf16_f32 v33, v28, v29
	s_mov_b32 s6, 0x500000
	global_store_dwordx4 v[46:47], v[30:33], off offset:256
	s_mov_b64 s[16:17], 0x500000
	v_cvt_pk_bf16_f32 v14, v14, v15
	v_add_co_u32_e32 v32, vcc, s6, v138
	v_lshl_add_u64 v[30:31], v[138:139], 0, s[16:17]
	s_nop 0
	v_addc_co_u32_e32 v33, vcc, 0, v139, vcc
	v_cvt_pk_bf16_f32 v15, v16, v17
	v_cvt_pk_bf16_f32 v16, v10, v11
	v_cvt_pk_bf16_f32 v17, v12, v13
	s_mov_b32 s6, 0x580000
	global_store_dwordx4 v[30:31], v[14:17], off offset:256
	s_mov_b64 s[16:17], 0x580000
	v_cvt_pk_bf16_f32 v126, v126, v127
	v_add_co_u32_e32 v16, vcc, s6, v138
	v_cvt_pk_bf16_f32 v127, v128, v129
	s_nop 0
	v_addc_co_u32_e32 v17, vcc, 0, v139, vcc
	v_cvt_pk_bf16_f32 v128, v122, v123
	v_cvt_pk_bf16_f32 v129, v124, v125
	v_cvt_pk_bf16_f32 v106, v118, v119
	v_cvt_pk_bf16_f32 v107, v120, v121
	v_cvt_pk_bf16_f32 v108, v114, v115
	v_cvt_pk_bf16_f32 v109, v116, v117
	v_cvt_pk_bf16_f32 v90, v102, v103
	v_cvt_pk_bf16_f32 v91, v104, v105
	v_cvt_pk_bf16_f32 v92, v98, v99
	v_cvt_pk_bf16_f32 v93, v100, v101
	v_cvt_pk_bf16_f32 v74, v86, v87
	v_cvt_pk_bf16_f32 v75, v88, v89
	v_cvt_pk_bf16_f32 v76, v82, v83
	v_cvt_pk_bf16_f32 v77, v84, v85
	v_cvt_pk_bf16_f32 v62, v66, v67
	v_cvt_pk_bf16_f32 v63, v68, v69
	v_cvt_pk_bf16_f32 v65, v60, v61
	v_cvt_pk_bf16_f32 v42, v54, v55
	v_cvt_pk_bf16_f32 v43, v56, v57
	v_cvt_pk_bf16_f32 v44, v50, v51
	v_cvt_pk_bf16_f32 v45, v52, v53
	v_cvt_pk_bf16_f32 v26, v38, v39
	v_cvt_pk_bf16_f32 v27, v40, v41
	v_cvt_pk_bf16_f32 v28, v34, v35
	v_cvt_pk_bf16_f32 v29, v36, v37
	v_lshl_add_u64 v[14:15], v[138:139], 0, s[16:17]
	v_cvt_pk_bf16_f32 v10, v22, v23
	v_cvt_pk_bf16_f32 v11, v24, v25
	v_cvt_pk_bf16_f32 v12, v18, v19
	v_cvt_pk_bf16_f32 v13, v20, v21
	v_cvt_pk_bf16_f32 v6, v6, v7
	v_cvt_pk_bf16_f32 v7, v8, v9
	v_cvt_pk_bf16_f32 v8, v2, v3
	v_cvt_pk_bf16_f32 v9, v4, v5
	s_andn2_b64 vcc, exec, s[2:3]
	s_mov_b64 s[2:3], -1
	global_store_dwordx4 v[138:139], v[126:129], off
	global_store_dwordx4 v[112:113], v[106:109], off
	global_store_dwordx4 v[96:97], v[90:93], off
	global_store_dwordx4 v[80:81], v[74:77], off
	global_store_dwordx4 v[58:59], v[62:65], off
	global_store_dwordx4 v[48:49], v[42:45], off
	global_store_dwordx4 v[32:33], v[26:29], off
	global_store_dwordx4 v[16:17], v[10:13], off
	global_store_dwordx4 v[14:15], v[6:9], off offset:256
	s_cbranch_vccnz .LBB0_160
	s_andn2_b64 vcc, exec, s[0:1]
	s_cbranch_vccnz .LBB0_159
	s_barrier
	s_branch .LBB0_159

.LBB0_404:
	v_add_u32_e32 v137, s65, v133
	v_add_u32_e32 v138, s67, v135
	v_ashrrev_i32_e32 v139, 31, v138
	v_mad_i64_i32 v[140:141], s[14:15], v137, s37, 0
	v_cvt_pk_bf16_f32 v110, v110, v111
	v_cvt_pk_bf16_f32 v111, v112, v113
	v_cvt_pk_bf16_f32 v112, v106, v107
	v_add_u32_e32 v106, 16, v137
	v_lshl_add_u64 v[140:141], v[140:141], 1, s[6:7]
	v_lshlrev_b64 v[138:139], 1, v[138:139]
	v_mad_i64_i32 v[106:107], s[14:15], v106, s37, 0
	v_cvt_pk_bf16_f32 v94, v94, v95
	v_cvt_pk_bf16_f32 v95, v96, v97
	v_cvt_pk_bf16_f32 v96, v90, v91
	v_add_u32_e32 v90, 32, v137
	v_lshl_add_u64 v[140:141], v[140:141], 0, v[138:139]
	v_cvt_pk_bf16_f32 v113, v108, v109
	v_lshl_add_u64 v[106:107], v[106:107], 1, s[6:7]
	v_mad_i64_i32 v[90:91], s[14:15], v90, s37, 0
	v_cvt_pk_bf16_f32 v78, v78, v79
	v_cvt_pk_bf16_f32 v79, v80, v81
	v_cvt_pk_bf16_f32 v80, v74, v75
	v_add_u32_e32 v74, 48, v137
	v_cvt_pk_bf16_f32 v126, v126, v127
	v_cvt_pk_bf16_f32 v127, v128, v129
	v_cvt_pk_bf16_f32 v128, v122, v123
	v_cvt_pk_bf16_f32 v129, v124, v125
	global_store_dwordx4 v[140:141], v[110:113], off offset:256
	v_cvt_pk_bf16_f32 v97, v92, v93
	v_lshl_add_u64 v[90:91], v[90:91], 1, s[6:7]
	v_lshl_add_u64 v[110:111], v[106:107], 0, v[138:139]
	v_mad_i64_i32 v[74:75], s[14:15], v74, s37, 0
	v_cvt_pk_bf16_f32 v70, v70, v71
	v_cvt_pk_bf16_f32 v71, v72, v73
	v_cvt_pk_bf16_f32 v72, v62, v63
	v_add_u32_e32 v62, 0x80, v137
	global_store_dwordx4 v[140:141], v[126:129], off
	v_cvt_pk_bf16_f32 v106, v118, v119
	v_cvt_pk_bf16_f32 v107, v120, v121
	v_cvt_pk_bf16_f32 v108, v114, v115
	v_cvt_pk_bf16_f32 v109, v116, v117
	global_store_dwordx4 v[110:111], v[94:97], off offset:256
	v_cvt_pk_bf16_f32 v81, v76, v77
	v_lshl_add_u64 v[74:75], v[74:75], 1, s[6:7]
	v_lshl_add_u64 v[94:95], v[90:91], 0, v[138:139]
	v_mad_i64_i32 v[62:63], s[14:15], v62, s37, 0
	v_cvt_pk_bf16_f32 v46, v46, v47
	v_cvt_pk_bf16_f32 v47, v48, v49
	v_cvt_pk_bf16_f32 v48, v42, v43
	v_add_u32_e32 v42, 0x90, v137
	global_store_dwordx4 v[110:111], v[106:109], off
	v_cvt_pk_bf16_f32 v90, v102, v103
	v_cvt_pk_bf16_f32 v91, v104, v105
	v_cvt_pk_bf16_f32 v92, v98, v99
	v_cvt_pk_bf16_f32 v93, v100, v101
	global_store_dwordx4 v[94:95], v[78:81], off offset:256
	v_cvt_pk_bf16_f32 v73, v64, v65
	v_lshl_add_u64 v[62:63], v[62:63], 1, s[6:7]
	v_lshl_add_u64 v[78:79], v[74:75], 0, v[138:139]
	v_mad_i64_i32 v[42:43], s[14:15], v42, s37, 0
	v_cvt_pk_bf16_f32 v30, v30, v31
	v_cvt_pk_bf16_f32 v31, v32, v33
	v_cvt_pk_bf16_f32 v32, v26, v27
	v_add_u32_e32 v26, 0xa0, v137
	global_store_dwordx4 v[94:95], v[90:93], off
	v_cvt_pk_bf16_f32 v74, v86, v87
	v_cvt_pk_bf16_f32 v75, v88, v89
	v_cvt_pk_bf16_f32 v76, v82, v83
	v_cvt_pk_bf16_f32 v77, v84, v85
	global_store_dwordx4 v[78:79], v[70:73], off offset:256
	v_cvt_pk_bf16_f32 v49, v44, v45
	v_lshl_add_u64 v[42:43], v[42:43], 1, s[6:7]
	v_lshl_add_u64 v[70:71], v[62:63], 0, v[138:139]
	v_mad_i64_i32 v[26:27], s[14:15], v26, s37, 0
	v_cvt_pk_bf16_f32 v14, v14, v15
	v_cvt_pk_bf16_f32 v15, v16, v17
	v_cvt_pk_bf16_f32 v16, v10, v11
	v_add_u32_e32 v10, 0xb0, v137
	global_store_dwordx4 v[78:79], v[74:77], off
	v_cvt_pk_bf16_f32 v62, v66, v67
	v_cvt_pk_bf16_f32 v63, v68, v69
	v_cvt_pk_bf16_f32 v64, v58, v59
	v_cvt_pk_bf16_f32 v65, v60, v61
	global_store_dwordx4 v[70:71], v[46:49], off offset:256
	v_cvt_pk_bf16_f32 v33, v28, v29
	v_lshl_add_u64 v[26:27], v[26:27], 1, s[6:7]
	v_lshl_add_u64 v[46:47], v[42:43], 0, v[138:139]
	v_mad_i64_i32 v[10:11], s[14:15], v10, s37, 0
	global_store_dwordx4 v[70:71], v[62:65], off
	v_cvt_pk_bf16_f32 v42, v54, v55
	v_cvt_pk_bf16_f32 v43, v56, v57
	v_cvt_pk_bf16_f32 v44, v50, v51
	v_cvt_pk_bf16_f32 v45, v52, v53
	global_store_dwordx4 v[46:47], v[30:33], off offset:256
	v_cvt_pk_bf16_f32 v17, v12, v13
	v_lshl_add_u64 v[10:11], v[10:11], 1, s[6:7]
	v_lshl_add_u64 v[30:31], v[26:27], 0, v[138:139]
	global_store_dwordx4 v[46:47], v[42:45], off
	v_cvt_pk_bf16_f32 v26, v38, v39
	v_cvt_pk_bf16_f32 v27, v40, v41
	v_cvt_pk_bf16_f32 v28, v34, v35
	v_cvt_pk_bf16_f32 v29, v36, v37
	global_store_dwordx4 v[30:31], v[14:17], off offset:256
	v_cvt_pk_bf16_f32 v12, v18, v19
	v_cvt_pk_bf16_f32 v13, v20, v21
	v_lshl_add_u64 v[14:15], v[10:11], 0, v[138:139]
	v_cvt_pk_bf16_f32 v10, v22, v23
	v_cvt_pk_bf16_f32 v11, v24, v25
	v_cvt_pk_bf16_f32 v6, v6, v7
	v_cvt_pk_bf16_f32 v7, v8, v9
	v_cvt_pk_bf16_f32 v8, v2, v3
	v_cvt_pk_bf16_f32 v9, v4, v5
	s_and_b64 vcc, exec, s[2:3]
	s_mov_b64 s[2:3], -1
	global_store_dwordx4 v[30:31], v[26:29], off
	global_store_dwordx4 v[14:15], v[10:13], off
	global_store_dwordx4 v[14:15], v[6:9], off offset:256
	s_cbranch_vccnz .LBB0_395
	s_andn2_b64 vcc, exec, s[4:5]
	s_cbranch_vccnz .LBB0_394
	s_barrier
	s_branch .LBB0_394

.LBB0_560:
	v_add_u32_e32 v138, s8, v133
	v_ashrrev_i32_e32 v139, 31, v138
	v_add_u32_e32 v140, s37, v135
	v_lshlrev_b64 v[138:139], 11, v[138:139]
	v_ashrrev_i32_e32 v141, 31, v140
	v_lshl_add_u64 v[138:139], s[6:7], 0, v[138:139]
	v_lshl_add_u64 v[138:139], v[140:141], 1, v[138:139]
	v_cvt_pk_bf16_f32 v110, v110, v111
	v_cvt_pk_bf16_f32 v111, v112, v113
	v_cvt_pk_bf16_f32 v112, v106, v107
	v_cvt_pk_bf16_f32 v113, v108, v109
	global_store_dwordx4 v[138:139], v[110:113], off offset:256
	s_mov_b64 s[18:19], 0x8000
	v_cvt_pk_bf16_f32 v94, v94, v95
	v_add_co_u32_e32 v112, vcc, s67, v138
	v_lshl_add_u64 v[110:111], v[138:139], 0, s[18:19]
	s_nop 0
	v_addc_co_u32_e32 v113, vcc, 0, v139, vcc
	v_cvt_pk_bf16_f32 v95, v96, v97
	v_cvt_pk_bf16_f32 v96, v90, v91
	v_cvt_pk_bf16_f32 v97, v92, v93
	s_mov_b32 s8, 0x10000
	global_store_dwordx4 v[110:111], v[94:97], off offset:256
	s_mov_b64 s[18:19], 0x10000
	v_cvt_pk_bf16_f32 v78, v78, v79
	v_add_co_u32_e32 v96, vcc, s8, v138
	v_lshl_add_u64 v[94:95], v[138:139], 0, s[18:19]
	s_nop 0
	v_addc_co_u32_e32 v97, vcc, 0, v139, vcc
	v_cvt_pk_bf16_f32 v79, v80, v81
	v_cvt_pk_bf16_f32 v80, v74, v75
	v_cvt_pk_bf16_f32 v81, v76, v77
	s_mov_b32 s8, 0x18000
	global_store_dwordx4 v[94:95], v[78:81], off offset:256
	s_mov_b64 s[18:19], 0x18000
	v_cvt_pk_bf16_f32 v70, v70, v71
	v_add_co_u32_e32 v80, vcc, s8, v138
	s_mov_b32 s8, 0x40000
	s_nop 0
	v_addc_co_u32_e32 v81, vcc, 0, v139, vcc
	v_lshl_add_u64 v[78:79], v[138:139], 0, s[18:19]
	v_cvt_pk_bf16_f32 v71, v72, v73
	v_cvt_pk_bf16_f32 v72, v62, v63
	v_cvt_pk_bf16_f32 v73, v64, v65
	s_mov_b64 s[18:19], 0x40000
	v_cvt_pk_bf16_f32 v64, v58, v59
	v_add_co_u32_e32 v58, vcc, s8, v138
	global_store_dwordx4 v[78:79], v[70:73], off offset:256
	s_nop 0
	v_addc_co_u32_e32 v59, vcc, 0, v139, vcc
	v_lshl_add_u64 v[70:71], v[138:139], 0, s[18:19]
	v_cvt_pk_bf16_f32 v46, v46, v47
	v_cvt_pk_bf16_f32 v47, v48, v49
	v_cvt_pk_bf16_f32 v48, v42, v43
	v_cvt_pk_bf16_f32 v49, v44, v45
	s_mov_b32 s8, 0x48000
	global_store_dwordx4 v[70:71], v[46:49], off offset:256
	s_mov_b64 s[18:19], 0x48000
	v_cvt_pk_bf16_f32 v30, v30, v31
	v_add_co_u32_e32 v48, vcc, s8, v138
	v_lshl_add_u64 v[46:47], v[138:139], 0, s[18:19]
	s_nop 0
	v_addc_co_u32_e32 v49, vcc, 0, v139, vcc
	v_cvt_pk_bf16_f32 v31, v32, v33
	v_cvt_pk_bf16_f32 v32, v26, v27
	v_cvt_pk_bf16_f32 v33, v28, v29
	s_mov_b32 s8, 0x50000
	global_store_dwordx4 v[46:47], v[30:33], off offset:256
	s_mov_b64 s[18:19], 0x50000
	v_cvt_pk_bf16_f32 v14, v14, v15
	v_add_co_u32_e32 v32, vcc, s8, v138
	v_lshl_add_u64 v[30:31], v[138:139], 0, s[18:19]
	s_nop 0
	v_addc_co_u32_e32 v33, vcc, 0, v139, vcc
	v_cvt_pk_bf16_f32 v15, v16, v17
	v_cvt_pk_bf16_f32 v16, v10, v11
	v_cvt_pk_bf16_f32 v17, v12, v13
	s_mov_b32 s8, 0x58000
	global_store_dwordx4 v[30:31], v[14:17], off offset:256
	s_mov_b64 s[18:19], 0x58000
	v_cvt_pk_bf16_f32 v126, v126, v127
	v_add_co_u32_e32 v16, vcc, s8, v138
	v_cvt_pk_bf16_f32 v127, v128, v129
	s_nop 0
	v_addc_co_u32_e32 v17, vcc, 0, v139, vcc
	v_cvt_pk_bf16_f32 v128, v122, v123
	v_cvt_pk_bf16_f32 v129, v124, v125
	v_cvt_pk_bf16_f32 v106, v118, v119
	v_cvt_pk_bf16_f32 v107, v120, v121
	v_cvt_pk_bf16_f32 v108, v114, v115
	v_cvt_pk_bf16_f32 v109, v116, v117
	v_cvt_pk_bf16_f32 v90, v102, v103
	v_cvt_pk_bf16_f32 v91, v104, v105
	v_cvt_pk_bf16_f32 v92, v98, v99
	v_cvt_pk_bf16_f32 v93, v100, v101
	v_cvt_pk_bf16_f32 v74, v86, v87
	v_cvt_pk_bf16_f32 v75, v88, v89
	v_cvt_pk_bf16_f32 v76, v82, v83
	v_cvt_pk_bf16_f32 v77, v84, v85
	v_cvt_pk_bf16_f32 v62, v66, v67
	v_cvt_pk_bf16_f32 v63, v68, v69
	v_cvt_pk_bf16_f32 v65, v60, v61
	v_cvt_pk_bf16_f32 v42, v54, v55
	v_cvt_pk_bf16_f32 v43, v56, v57
	v_cvt_pk_bf16_f32 v44, v50, v51
	v_cvt_pk_bf16_f32 v45, v52, v53
	v_cvt_pk_bf16_f32 v26, v38, v39
	v_cvt_pk_bf16_f32 v27, v40, v41
	v_cvt_pk_bf16_f32 v28, v34, v35
	v_cvt_pk_bf16_f32 v29, v36, v37
	v_lshl_add_u64 v[14:15], v[138:139], 0, s[18:19]
	v_cvt_pk_bf16_f32 v10, v22, v23
	v_cvt_pk_bf16_f32 v11, v24, v25
	v_cvt_pk_bf16_f32 v12, v18, v19
	v_cvt_pk_bf16_f32 v13, v20, v21
	v_cvt_pk_bf16_f32 v6, v6, v7
	v_cvt_pk_bf16_f32 v7, v8, v9
	v_cvt_pk_bf16_f32 v8, v2, v3
	v_cvt_pk_bf16_f32 v9, v4, v5
	s_andn2_b64 vcc, exec, s[2:3]
	s_mov_b64 s[2:3], -1
	global_store_dwordx4 v[138:139], v[126:129], off
	global_store_dwordx4 v[112:113], v[106:109], off
	global_store_dwordx4 v[96:97], v[90:93], off
	global_store_dwordx4 v[80:81], v[74:77], off
	global_store_dwordx4 v[58:59], v[62:65], off
	global_store_dwordx4 v[48:49], v[42:45], off
	global_store_dwordx4 v[32:33], v[26:29], off
	global_store_dwordx4 v[16:17], v[10:13], off
	global_store_dwordx4 v[14:15], v[6:9], off offset:256
	s_cbranch_vccnz .LBB0_549
	s_andn2_b64 vcc, exec, s[4:5]
	s_cbranch_vccnz .LBB0_548
	s_barrier
	s_branch .LBB0_548
